# non-temporal (nt) hint on the once-read f32 expert-weight loads of the per-layer expert conversion pass (201 MB per layer that is never read again), so they do not displace the activations just writte
# speedup vs baseline: 1.0050x; 1.0037x over previous
; #define LAS __attribute__((address_space(3)))
; __device__ __forceinline__ const float* IN(KArgs a, int i) { return (const float*)a->in[i]; }
; #define a launder(kargs)
; __device__ __forceinline__ void transpose_item(const float* W, int ldw, int k0, int n0, bf16_t* dstrow0, int ldt, LAS float* scr, int lane) {
; #pragma unroll 8
;     for (int i = 0; i < 32; ++i) { const int kk = 2 * i + (lane >> 5); scr[kk * 33 + (lane & 31)] = W[(size_t)(k0 + kk) * ldw + n0 + (lane & 31)]; }
; __device__ __forceinline__ void convert_experts(Frame& F, KArgs a, int L) {
;     ...
;     for (int it = F.gw; it < 3 * 8192; it += F.NGW) {
;         const int which = it >> 13, r = it & 8191, e = r >> 9, q = r & 511, kb = q >> 5, nb = q & 31, n0 = nb * 32;
;         const float* src = IN(a, which == 0 ? I_WG : (which == 1 ? I_WU : I_WDN)) + ((size_t)(L * 16 + e)) * 1024 * 1024;
;         bf16_t* dst = (which == 2) ? wd + ((size_t)e * 1024 + n0) * 1024 : wgu + ((size_t)e * 2048 + (n0 >> 7) * 256 + (n0 & 127) + (which == 1 ? 128 : 0)) * 1024;
;         transpose_item(src, 1024, kb * 64, n0, dst, 1024, scr, F.lane);
.LBB0_251:
	s_lshl_b32 s23, s10, 1
	s_lshl_b32 s25, s15, 1
	v_or_b32_e32 v15, s25, v2
	s_add_i32 s26, s23, 4
	s_add_i32 s27, s25, 4
	s_add_i32 s29, s25, 8
	v_add_u32_e32 v194, s11, v15
	v_or_b32_e32 v17, s26, v1
	v_or_b32_e32 v29, s27, v2
	v_mov_b32_e32 v23, v195
	v_or_b32_e32 v5, s23, v1
	s_add_i32 s31, s25, 12
	v_or_b32_e32 v45, s29, v2
	v_lshlrev_b64 v[38:39], 12, v[194:195]
	v_add_u32_e32 v22, s14, v17
	v_add_u32_e32 v194, s11, v29
	v_mov_b32_e32 v21, v195
	s_add_i32 s28, s23, 8
	s_add_i32 s30, s23, 12
	s_add_i32 s35, s25, 16
	v_add_u32_e32 v20, s14, v5
	v_or_b32_e32 v47, s31, v2
	v_lshlrev_b64 v[22:23], 12, v[22:23]
	v_lshlrev_b64 v[40:41], 12, v[194:195]
	v_add_u32_e32 v194, s11, v45
	s_add_i32 s37, s25, 20
	v_or_b32_e32 v44, s28, v1
	v_or_b32_e32 v46, s30, v1
	v_or_b32_e32 v49, s35, v2
	v_lshlrev_b64 v[20:21], 12, v[20:21]
	v_lshl_add_u64 v[38:39], v[18:19], 0, v[38:39]
	v_lshl_add_u64 v[22:23], v[18:19], 0, v[22:23]
	v_lshlrev_b64 v[42:43], 12, v[194:195]
	v_add_u32_e32 v194, s11, v47
	v_mov_b32_e32 v25, v195
	v_mov_b32_e32 v27, v195
	s_add_i32 s34, s23, 16
	s_add_i32 s36, s23, 20
	s_add_i32 s40, s25, 24
	v_or_b32_e32 v51, s37, v2
	v_add_u32_e32 v24, s14, v44
	v_add_u32_e32 v26, s14, v46
	v_lshl_add_u64 v[20:21], v[18:19], 0, v[20:21]
	v_lshl_add_u64 v[40:41], v[18:19], 0, v[40:41]
	global_load_dword v56, v[38:39], off nt
	global_load_dword v57, v[20:21], off nt
	global_load_dword v58, v[40:41], off nt
	global_load_dword v59, v[22:23], off nt
	v_lshlrev_b64 v[22:23], 12, v[194:195]
	v_add_u32_e32 v194, s11, v49
	s_add_i32 s38, s23, 24
	s_add_i32 s23, s23, 28
	s_add_i32 s25, s25, 28
	v_or_b32_e32 v48, s34, v1
	v_or_b32_e32 v50, s36, v1
	v_or_b32_e32 v53, s40, v2
	v_lshlrev_b64 v[24:25], 12, v[24:25]
	v_lshlrev_b64 v[26:27], 12, v[26:27]
	v_lshl_add_u64 v[20:21], v[18:19], 0, v[42:43]
	v_lshl_add_u64 v[22:23], v[18:19], 0, v[22:23]
	v_lshlrev_b64 v[38:39], 12, v[194:195]
	v_add_u32_e32 v194, s11, v51
	v_mov_b32_e32 v31, v195
	v_mov_b32_e32 v33, v195
	v_or_b32_e32 v52, s38, v1
	v_or_b32_e32 v54, s23, v1
	v_or_b32_e32 v55, s25, v2
	v_add_u32_e32 v30, s14, v48
	v_add_u32_e32 v32, s14, v50
	v_lshl_add_u64 v[24:25], v[18:19], 0, v[24:25]
	v_lshl_add_u64 v[26:27], v[18:19], 0, v[26:27]
	global_load_dword v60, v[20:21], off nt
	global_load_dword v61, v[24:25], off nt
	global_load_dword v62, v[22:23], off nt
	global_load_dword v63, v[26:27], off nt
	v_lshlrev_b64 v[22:23], 12, v[194:195]
	v_add_u32_e32 v194, s11, v53
	v_mov_b32_e32 v35, v195
	v_mov_b32_e32 v37, v195
	v_add_u32_e32 v34, s14, v52
	v_add_u32_e32 v36, s14, v54
	v_lshlrev_b64 v[30:31], 12, v[30:31]
	v_lshlrev_b64 v[32:33], 12, v[32:33]
	v_lshl_add_u64 v[20:21], v[18:19], 0, v[38:39]
	v_lshl_add_u64 v[22:23], v[18:19], 0, v[22:23]
	v_lshlrev_b64 v[24:25], 12, v[194:195]
	v_add_u32_e32 v194, s11, v55
	v_lshlrev_b64 v[34:35], 12, v[34:35]
	v_lshlrev_b64 v[36:37], 12, v[36:37]
	v_lshl_add_u64 v[30:31], v[18:19], 0, v[30:31]
	v_lshl_add_u64 v[32:33], v[18:19], 0, v[32:33]
	global_load_dword v64, v[20:21], off nt
	global_load_dword v65, v[30:31], off nt
	global_load_dword v66, v[22:23], off nt
	global_load_dword v67, v[32:33], off nt
	v_lshl_add_u64 v[20:21], v[18:19], 0, v[24:25]
	v_lshlrev_b64 v[22:23], 12, v[194:195]
	v_lshl_add_u64 v[34:35], v[18:19], 0, v[34:35]
	v_lshl_add_u64 v[36:37], v[18:19], 0, v[36:37]
	v_lshl_add_u64 v[22:23], v[18:19], 0, v[22:23]
	global_load_dword v68, v[20:21], off nt
	global_load_dword v69, v[34:35], off nt
	global_load_dword v70, v[22:23], off nt
	global_load_dword v71, v[36:37], off nt
	s_add_i32 s15, s15, 16
	s_add_i32 s10, s10, 16
	s_add_i32 s22, s22, -16
	v_mad_u64_u32 v[20:21], s[26:27], v15, s75, v[4:5]
	s_cmp_lg_u32 s22, 0
	v_mad_u64_u32 v[22:23], s[26:27], v5, s75, v[4:5]
	v_mad_u64_u32 v[24:25], s[26:27], v29, s75, v[4:5]
	v_mad_u64_u32 v[26:27], s[26:27], v17, s75, v[4:5]
	v_mad_u64_u32 v[30:31], s[26:27], v45, s75, v[4:5]
	v_mad_u64_u32 v[32:33], s[26:27], v44, s75, v[4:5]
	v_mad_u64_u32 v[34:35], s[26:27], v47, s75, v[4:5]
	v_mad_u64_u32 v[36:37], s[26:27], v46, s75, v[4:5]
	v_mad_u64_u32 v[38:39], s[26:27], v49, s75, v[4:5]
	v_mad_u64_u32 v[40:41], s[26:27], v48, s75, v[4:5]
	v_mad_u64_u32 v[42:43], s[26:27], v51, s75, v[4:5]
	v_mad_u64_u32 v[44:45], s[26:27], v50, s75, v[4:5]
	v_mad_u64_u32 v[46:47], s[26:27], v53, s75, v[4:5]
	v_mad_u64_u32 v[48:49], s[26:27], v52, s75, v[4:5]
	v_mad_u64_u32 v[50:51], s[26:27], v55, s75, v[4:5]
	v_mad_u64_u32 v[52:53], s[26:27], v54, s75, v[4:5]
	s_waitcnt vmcnt(15)
	ds_write_b32 v20, v56 offset:61440
	s_waitcnt vmcnt(14)
	ds_write_b32 v22, v57 offset:61440
	s_waitcnt vmcnt(13)
	ds_write_b32 v24, v58 offset:61440
	s_waitcnt vmcnt(12)
	ds_write_b32 v26, v59 offset:61440
	s_waitcnt vmcnt(11)
	ds_write_b32 v30, v60 offset:61440
	s_waitcnt vmcnt(10)
	ds_write_b32 v32, v61 offset:61440
	s_waitcnt vmcnt(9)
	ds_write_b32 v34, v62 offset:61440
	s_waitcnt vmcnt(8)
	ds_write_b32 v36, v63 offset:61440
	s_waitcnt vmcnt(7)
	ds_write_b32 v38, v64 offset:61440
	s_waitcnt vmcnt(6)
	ds_write_b32 v40, v65 offset:61440
	s_waitcnt vmcnt(5)
	ds_write_b32 v42, v66 offset:61440
	s_waitcnt vmcnt(4)
	ds_write_b32 v44, v67 offset:61440
	s_waitcnt vmcnt(3)
	ds_write_b32 v46, v68 offset:61440
	s_waitcnt vmcnt(2)
	ds_write_b32 v48, v69 offset:61440
	s_waitcnt vmcnt(1)
	ds_write_b32 v50, v70 offset:61440
	s_waitcnt vmcnt(0)
	ds_write_b32 v52, v71 offset:61440
	s_cbranch_scc1 .LBB0_251
; #define LAS __attribute__((address_space(3)))
; __device__ __forceinline__ unsigned cvtpk(float lo, float hi) { f32x2 v = {lo, hi}; bf16x2_t b = __builtin_convertvector(v, bf16x2_t); return __builtin_bit_cast(unsigned, b); }
; #define LDS_WAIT() asm volatile("s_waitcnt lgkmcnt(0)" ::: "memory")
; __device__ __forceinline__ const float* IN(KArgs a, int i) { return (const float*)a->in[i]; }
; #define a launder(kargs)
; __device__ __forceinline__ void transpose_item(const float* W, int ldw, int k0, int n0, bf16_t* dstrow0, int ldt, LAS float* scr, int lane) {
;     ...
;     const int c = lane & 7;
; #pragma unroll
;     for (int j = 0; j < 4; ++j) { const int n = (lane >> 3) + 8 * j; const LAS float* s = scr + (8 * c) * 33 + n;
;         u32x4 o; o.x = cvtpk(s[0 * 33], s[1 * 33]); o.y = cvtpk(s[2 * 33], s[3 * 33]); o.z = cvtpk(s[4 * 33], s[5 * 33]); o.w = cvtpk(s[6 * 33], s[7 * 33]);
;         *(u32x4*)(dstrow0 + (size_t)n * ldt + k0 + 8 * c) = o; }
;     LDS_WAIT(); asm volatile("" ::: "memory");
; __device__ __forceinline__ void convert_experts(Frame& F, KArgs a, int L) {
;     ...
;     for (int it = F.gw; it < 3 * 8192; it += F.NGW) {
;         const int which = it >> 13, r = it & 8191, e = r >> 9, q = r & 511, kb = q >> 5, nb = q & 31, n0 = nb * 32;
;         const float* src = IN(a, which == 0 ? I_WG : (which == 1 ? I_WU : I_WDN)) + ((size_t)(L * 16 + e)) * 1024 * 1024;
;         bf16_t* dst = (which == 2) ? wd + ((size_t)e * 1024 + n0) * 1024 : wgu + ((size_t)e * 2048 + (n0 >> 7) * 256 + (n0 & 127) + (which == 1 ? 128 : 0)) * 1024;
;         transpose_item(src, 1024, kb * 64, n0, dst, 1024, scr, F.lane);
	s_waitcnt lgkmcnt(0)
	v_add_u32_e32 v5, 0xf000, v3
	ds_read2_b32 v[22:23], v5 offset0:33 offset1:41
	ds_read2_b32 v[24:25], v5 offset1:8
	ds_read2_b32 v[26:27], v5 offset0:66 offset1:74
	ds_read2_b32 v[30:31], v5 offset0:99 offset1:107
	ds_read2_b32 v[32:33], v5 offset0:132 offset1:140
	ds_read2_b32 v[34:35], v5 offset0:165 offset1:173
	ds_read2_b32 v[36:37], v5 offset0:198 offset1:206
	ds_read2_b32 v[38:39], v5 offset0:231 offset1:239
	s_lshl_b32 s10, s11, 1
	s_add_u32 s8, s8, s10
	s_addc_u32 s9, s9, 0
	v_mov_b32_e32 v17, v195
	v_lshl_add_u64 v[40:41], s[8:9], 0, v[16:17]
	s_waitcnt lgkmcnt(6)
	v_cvt_pk_bf16_f32 v18, v24, v22
	s_waitcnt lgkmcnt(4)
	v_cvt_pk_bf16_f32 v19, v26, v30
	s_waitcnt lgkmcnt(2)
	v_cvt_pk_bf16_f32 v20, v32, v34
	s_waitcnt lgkmcnt(0)
	v_cvt_pk_bf16_f32 v21, v36, v38
	v_lshl_add_u64 v[42:43], v[40:41], 0, v[6:7]
	global_store_dwordx4 v[42:43], v[18:21], off
	s_add_i32 s21, s21, s3
	s_cmpk_lt_i32 s21, 0x6000
	v_cvt_pk_bf16_f32 v18, v25, v23
	v_cvt_pk_bf16_f32 v19, v27, v31
	v_cvt_pk_bf16_f32 v20, v33, v35
	v_cvt_pk_bf16_f32 v21, v37, v39
	ds_read2_b32 v[24:25], v5 offset0:49 offset1:57
	ds_read2_b32 v[26:27], v5 offset0:16 offset1:24
	ds_read2_b32 v[30:31], v5 offset0:82 offset1:90
	ds_read2_b32 v[32:33], v5 offset0:115 offset1:123
	ds_read2_b32 v[34:35], v5 offset0:148 offset1:156
	ds_read2_b32 v[36:37], v5 offset0:181 offset1:189
	ds_read2_b32 v[38:39], v5 offset0:214 offset1:222
	ds_read2_b32 v[42:43], v5 offset0:247 offset1:255
	v_lshl_add_u64 v[22:23], v[40:41], 0, v[8:9]
	global_store_dwordx4 v[22:23], v[18:21], off
	v_lshl_add_u64 v[22:23], v[40:41], 0, v[10:11]
	s_waitcnt lgkmcnt(6)
	v_cvt_pk_bf16_f32 v18, v26, v24
	s_waitcnt lgkmcnt(4)
	v_cvt_pk_bf16_f32 v19, v30, v32
	s_waitcnt lgkmcnt(2)
	v_cvt_pk_bf16_f32 v20, v34, v36
	s_waitcnt lgkmcnt(0)
	v_cvt_pk_bf16_f32 v21, v38, v42
	global_store_dwordx4 v[22:23], v[18:21], off
	v_lshl_add_u64 v[22:23], v[40:41], 0, v[12:13]
	s_nop 0
	v_cvt_pk_bf16_f32 v18, v27, v25
	v_cvt_pk_bf16_f32 v19, v31, v33
	v_cvt_pk_bf16_f32 v20, v35, v37
	v_cvt_pk_bf16_f32 v21, v39, v43
	global_store_dwordx4 v[22:23], v[18:21], off
	s_waitcnt lgkmcnt(0)
	s_cbranch_scc1 .LBB0_246
